# Q and last-G weight fragments read early into idle score registers so barrier B's lgkmcnt(0) has no fresh LDS reads to wait for (sync unchanged)
# speedup vs baseline: 1.0125x; 1.0125x over previous
.LBB1_59:
	s_setprio 0
	s_nop 10
	v_rcp_f32_e32 v8, v82
	v_cvt_f32_f16_sdwa v5, v229 dst_sel:DWORD dst_unused:UNUSED_PAD src0_sel:WORD_1
	v_cvt_f32_f16_e32 v4, v229
	v_cvt_f32_f16_sdwa v7, v230 dst_sel:DWORD dst_unused:UNUSED_PAD src0_sel:WORD_1
	v_cvt_f32_f16_e32 v6, v230
	v_cvt_f32_f16_sdwa v11, v232 dst_sel:DWORD dst_unused:UNUSED_PAD src0_sel:WORD_1
	v_cvt_f32_f16_e32 v10, v232
	v_cvt_f32_f16_sdwa v13, v234 dst_sel:DWORD dst_unused:UNUSED_PAD src0_sel:WORD_1
	v_cvt_f32_f16_e32 v12, v234
	v_pk_mul_f32 v[4:5], v[8:9], v[4:5] op_sel_hi:[0,1]
	v_pk_mul_f32 v[6:7], v[8:9], v[6:7] op_sel_hi:[0,1]
	v_pk_mul_f32 v[4:5], v[98:99], v[4:5]
	v_pk_mul_f32 v[6:7], v[100:101], v[6:7]
	v_cvt_pk_f16_f32 v4, v4, v5
	v_cvt_pk_f16_f32 v5, v6, v7
	v_pk_mul_f32 v[6:7], v[8:9], v[10:11] op_sel_hi:[0,1]
	v_pk_mul_f32 v[10:11], v[8:9], v[12:13] op_sel_hi:[0,1]
	v_pk_mul_f32 v[6:7], v[102:103], v[6:7]
	v_pk_mul_f32 v[10:11], v[104:105], v[10:11]
	v_cvt_pk_f16_f32 v6, v6, v7
	v_cvt_pk_f16_f32 v7, v10, v11
	v_cvt_f32_f16_sdwa v11, v228 dst_sel:DWORD dst_unused:UNUSED_PAD src0_sel:WORD_1
	v_cvt_f32_f16_e32 v10, v228
	ds_write_b128 v227, v[4:7]
	v_cvt_f32_f16_sdwa v7, v231 dst_sel:DWORD dst_unused:UNUSED_PAD src0_sel:WORD_1
	v_cvt_f32_f16_e32 v6, v231
	v_pk_mul_f32 v[4:5], v[8:9], v[10:11] op_sel_hi:[0,1]
	v_cvt_f32_f16_sdwa v11, v233 dst_sel:DWORD dst_unused:UNUSED_PAD src0_sel:WORD_1
	v_cvt_f32_f16_e32 v10, v233
	v_cvt_f32_f16_sdwa v13, v235 dst_sel:DWORD dst_unused:UNUSED_PAD src0_sel:WORD_1
	v_cvt_f32_f16_e32 v12, v235
	v_pk_mul_f32 v[6:7], v[8:9], v[6:7] op_sel_hi:[0,1]
	v_pk_mul_f32 v[4:5], v[4:5], v[106:107]
	v_pk_mul_f32 v[6:7], v[6:7], v[108:109]
	v_cvt_pk_f16_f32 v4, v4, v5
	v_cvt_pk_f16_f32 v5, v6, v7
	v_pk_mul_f32 v[6:7], v[8:9], v[10:11] op_sel_hi:[0,1]
	v_pk_mul_f32 v[8:9], v[8:9], v[12:13] op_sel_hi:[0,1]
	v_pk_mul_f32 v[6:7], v[6:7], v[110:111]
	v_pk_mul_f32 v[8:9], v[8:9], v[112:113]
	v_cvt_pk_f16_f32 v6, v6, v7
	v_cvt_pk_f16_f32 v7, v8, v9
	s_and_b64 vcc, exec, s[16:17]
	ds_write_b128 v227, v[4:7] offset:1024
	s_waitcnt vmcnt(0) lgkmcnt(2)
	s_barrier
	s_cbranch_vccnz .LBB1_5
	ds_read_b128 v[4:7], v206 offset:8192
	ds_read_b128 v[8:11], v206 offset:9216
	s_waitcnt lgkmcnt(1)
	v_mfma_f32_32x32x16_f16 v[114:129], v[4:7], v[130:133], 0
	ds_read_b128 v[4:7], v206 offset:16384
	ds_read_b128 v[12:15], v206 offset:17408
	s_waitcnt lgkmcnt(1)
	v_mfma_f32_32x32x16_f16 v[98:113], v[130:133], v[4:7], 0
	v_mfma_f32_32x32x16_f16 v[114:129], v[8:11], v[134:137], v[114:129]
	ds_read_b128 v[4:7], v206 offset:10240
	ds_read_b128 v[8:11], v206 offset:11264
	s_waitcnt lgkmcnt(2)
	v_mfma_f32_32x32x16_f16 v[98:113], v[134:137], v[12:15], v[98:113]
	s_waitcnt lgkmcnt(1)
	v_mfma_f32_32x32x16_f16 v[114:129], v[4:7], v[138:141], v[114:129]
	ds_read_b128 v[4:7], v206 offset:18432
	ds_read_b128 v[12:15], v206 offset:19456
	s_waitcnt lgkmcnt(1)
	v_mfma_f32_32x32x16_f16 v[98:113], v[138:141], v[4:7], v[98:113]
	v_mfma_f32_32x32x16_f16 v[114:129], v[8:11], v[142:145], v[114:129]
	ds_read_b128 v[4:7], v206 offset:12288
	ds_read_b128 v[8:11], v206 offset:13312
	s_waitcnt lgkmcnt(2)
	v_mfma_f32_32x32x16_f16 v[98:113], v[142:145], v[12:15], v[98:113]
	s_waitcnt lgkmcnt(1)
	v_mfma_f32_32x32x16_f16 v[114:129], v[4:7], v[146:149], v[114:129]
	ds_read_b128 v[4:7], v206 offset:20480
	ds_read_b128 v[12:15], v206 offset:21504
	s_waitcnt lgkmcnt(1)
	v_mfma_f32_32x32x16_f16 v[98:113], v[146:149], v[4:7], v[98:113]
	v_mfma_f32_32x32x16_f16 v[114:129], v[8:11], v[150:153], v[114:129]
	ds_read_b128 v[4:7], v206 offset:14336
	ds_read_b128 v[8:11], v206 offset:15360
	s_waitcnt lgkmcnt(2)
	v_mfma_f32_32x32x16_f16 v[98:113], v[150:153], v[12:15], v[98:113]
	s_waitcnt lgkmcnt(1)
	v_mfma_f32_32x32x16_f16 v[114:129], v[4:7], v[154:157], v[114:129]
	ds_read_b128 v[4:7], v206 offset:22528
	ds_read_b128 v[12:15], v206 offset:23552
	s_waitcnt lgkmcnt(1)
	v_mfma_f32_32x32x16_f16 v[98:113], v[154:157], v[4:7], v[98:113]
	v_mfma_f32_32x32x16_f16 v[114:129], v[8:11], v[158:161], v[114:129]
	ds_read_b128 v[4:7], v206 offset:24576
	ds_read_b128 v[8:11], v206 offset:25600
	s_waitcnt lgkmcnt(1)
	v_mfma_f32_32x32x16_f16 v[82:97], v[4:7], v[130:133], 0
	global_load_dwordx4 v[4:7], v[220:221], off
	s_nop 6
	v_cvt_pk_f16_f32 v121, v120, v121
	v_cvt_pk_f16_f32 v120, v118, v119
	v_cvt_pk_f16_f32 v119, v116, v117
	v_cvt_pk_f16_f32 v118, v114, v115
	v_cvt_pk_f16_f32 v117, v128, v129
	v_cvt_pk_f16_f32 v116, v126, v127
	s_waitcnt lgkmcnt(0)
	ds_read_b128 v[18:21], v206
	ds_read_b128 v[22:25], v206 offset:1024
	ds_read_b128 v[26:29], v206 offset:2048
	ds_read_b128 v[30:33], v206 offset:3072
	ds_read_b128 v[34:37], v206 offset:4096
	ds_read_b128 v[38:41], v206 offset:5120
	ds_read_b128 v[42:45], v206 offset:6144
	ds_read_b128 v[46:49], v206 offset:7168
	ds_read_b128 v[50:53], v206 offset:31744
	v_mfma_f32_32x32x16_f16 v[82:97], v[8:11], v[134:137], v[82:97]
	v_cvt_pk_f16_f32 v115, v124, v125
	v_cvt_pk_f16_f32 v114, v122, v123
	v_mfma_f32_32x32x16_f16 v[98:113], v[158:161], v[12:15], v[98:113]
	ds_read_b128 v[8:11], v206 offset:26624
	ds_read_b128 v[12:15], v206 offset:27648
	ds_read_b128 v[196:199], v206 offset:28672
	ds_write_b128 v209, v[114:117] offset:33792
	global_load_dwordx4 v[114:117], v[220:221], off offset:96
	ds_write_b128 v209, v[118:121] offset:32768
	ds_read_b128 v[118:121], v206 offset:29696
	s_nop 4
	v_cvt_pk_f16_f32 v105, v104, v105
	s_waitcnt lgkmcnt(5)
	v_mfma_f32_32x32x16_f16 v[82:97], v[8:11], v[138:141], v[82:97]
	global_load_dwordx4 v[8:11], v[220:221], off offset:32
	v_cvt_pk_f16_f32 v104, v102, v103
	v_cvt_pk_f16_f32 v103, v100, v101
	v_cvt_pk_f16_f32 v102, v98, v99
	ds_read_b128 v[98:101], v206 offset:30720
	ds_write_b128 v209, v[102:105] offset:49152
	v_cvt_pk_f16_f32 v103, v108, v109
	s_waitcnt lgkmcnt(6)
	v_mfma_f32_32x32x16_f16 v[82:97], v[12:15], v[142:145], v[82:97]
	global_load_dwordx4 v[12:15], v[220:221], off offset:64
	v_cvt_pk_f16_f32 v102, v106, v107
	v_cvt_pk_f16_f32 v105, v112, v113
	v_cvt_pk_f16_f32 v104, v110, v111
	ds_write_b128 v209, v[102:105] offset:50176
	s_waitcnt lgkmcnt(6)
	v_mfma_f32_32x32x16_f16 v[82:97], v[196:199], v[146:149], v[82:97]
	s_waitcnt lgkmcnt(3)
	v_mfma_f32_32x32x16_f16 v[82:97], v[118:121], v[150:153], v[82:97]
	s_waitcnt lgkmcnt(2)
	v_mfma_f32_32x32x16_f16 v[82:97], v[98:101], v[154:157], v[82:97]
	s_waitcnt lgkmcnt(0)
	s_barrier
	v_mfma_f32_32x32x16_f16 v[82:97], v[50:53], v[158:161], v[82:97]
	v_mfma_f32_32x32x16_f16 v[98:113], v[18:21], v[130:133], 0
	s_waitcnt vmcnt(3)
	s_nop 9
	v_add_f32_e32 v1, v82, v4
	v_mfma_f32_32x32x16_f16 v[98:113], v[22:25], v[134:137], v[98:113]
	v_add_f32_e32 v3, v5, v83
	v_add_f32_e32 v4, v6, v84
	v_add_f32_e32 v5, v7, v85
	v_mul_f32_e32 v1, 0xbfb8aa3b, v1
	v_mul_f32_e32 v3, 0xbfb8aa3b, v3
	v_mul_f32_e32 v4, 0xbfb8aa3b, v4
	v_mul_f32_e32 v5, 0xbfb8aa3b, v5
	v_mfma_f32_32x32x16_f16 v[98:113], v[26:29], v[138:141], v[98:113]
	v_exp_f32_e32 v1, v1
	v_exp_f32_e32 v3, v3
	v_exp_f32_e32 v4, v4
	v_exp_f32_e32 v5, v5
	v_add_f32_e32 v1, 1.0, v1
	v_add_f32_e32 v3, 1.0, v3
	v_add_f32_e32 v4, 1.0, v4
	v_mfma_f32_32x32x16_f16 v[98:113], v[30:33], v[142:145], v[98:113]
	v_add_f32_e32 v5, 1.0, v5
	s_waitcnt vmcnt(2)
	v_add_f32_e32 v16, v116, v96
	v_add_f32_e32 v17, v117, v97
	v_mul_f32_e32 v16, 0xbfb8aa3b, v16
	v_mul_f32_e32 v17, 0xbfb8aa3b, v17
	v_exp_f32_e32 v16, v16
	v_exp_f32_e32 v17, v17
	v_mfma_f32_32x32x16_f16 v[98:113], v[34:37], v[146:149], v[98:113]
	s_waitcnt vmcnt(1)
	v_add_f32_e32 v6, v86, v8
	v_add_f32_e32 v7, v9, v87
	v_add_f32_e32 v8, v10, v88
	v_add_f32_e32 v9, v11, v89
	v_mul_f32_e32 v6, 0xbfb8aa3b, v6
	v_mul_f32_e32 v7, 0xbfb8aa3b, v7
	v_mul_f32_e32 v8, 0xbfb8aa3b, v8
	v_mfma_f32_32x32x16_f16 v[98:113], v[38:41], v[150:153], v[98:113]
	s_waitcnt vmcnt(0)
	v_add_f32_e32 v10, v90, v12
	v_add_f32_e32 v11, v13, v91
	v_add_f32_e32 v12, v14, v92
	v_add_f32_e32 v13, v15, v93
	v_add_f32_e32 v14, v94, v114
	v_add_f32_e32 v15, v115, v95
	v_mul_f32_e32 v9, 0xbfb8aa3b, v9
	v_mfma_f32_32x32x16_f16 v[98:113], v[42:45], v[154:157], v[98:113]
	v_mul_f32_e32 v10, 0xbfb8aa3b, v10
	v_mul_f32_e32 v11, 0xbfb8aa3b, v11
	v_mul_f32_e32 v12, 0xbfb8aa3b, v12
	v_mul_f32_e32 v13, 0xbfb8aa3b, v13
	v_mul_f32_e32 v14, 0xbfb8aa3b, v14
	v_mul_f32_e32 v15, 0xbfb8aa3b, v15
	v_exp_f32_e32 v6, v6
	v_exp_f32_e32 v7, v7
	v_exp_f32_e32 v8, v8
	v_exp_f32_e32 v9, v9
	v_exp_f32_e32 v10, v10
	v_exp_f32_e32 v11, v11
	v_exp_f32_e32 v12, v12
	v_exp_f32_e32 v13, v13
	v_exp_f32_e32 v14, v14
	v_exp_f32_e32 v15, v15
	v_mfma_f32_32x32x16_f16 v[98:113], v[46:49], v[158:161], v[98:113]
	v_add_f32_e32 v6, 1.0, v6
	v_add_f32_e32 v7, 1.0, v7
	v_add_f32_e32 v8, 1.0, v8
	v_add_f32_e32 v9, 1.0, v9
	v_add_f32_e32 v10, 1.0, v10
	v_add_f32_e32 v11, 1.0, v11
	v_add_f32_e32 v12, 1.0, v12
	v_add_f32_e32 v13, 1.0, v13
	v_add_f32_e32 v14, 1.0, v14
	v_add_f32_e32 v15, 1.0, v15
	v_add_f32_e32 v16, 1.0, v16
	v_add_f32_e32 v17, 1.0, v17
	v_rcp_f32_e32 v1, v1
	v_rcp_f32_e32 v3, v3
	v_rcp_f32_e32 v4, v4
	v_rcp_f32_e32 v5, v5
	v_rcp_f32_e32 v6, v6
	v_rcp_f32_e32 v7, v7
	v_rcp_f32_e32 v8, v8
	v_rcp_f32_e32 v9, v9
	v_rcp_f32_e32 v10, v10
	v_rcp_f32_e32 v11, v11
	v_rcp_f32_e32 v12, v12
	v_rcp_f32_e32 v13, v13
	v_rcp_f32_e32 v14, v14
	v_rcp_f32_e32 v15, v15
	v_rcp_f32_e32 v16, v16
	v_rcp_f32_e32 v17, v17
	v_cvt_pk_f16_f32 v228, v10, v11
	v_cvt_pk_f16_f32 v231, v12, v13
	v_cvt_pk_f16_f32 v233, v14, v15
	v_cvt_pk_f16_f32 v235, v16, v17
	v_cvt_pk_f16_f32 v229, v1, v3
	v_cvt_pk_f16_f32 v230, v4, v5
	v_cvt_pk_f16_f32 v232, v6, v7
	v_cvt_pk_f16_f32 v234, v8, v9
	v_cvt_pk_f16_f32 v202, v106, v107
	v_cvt_pk_f16_f32 v203, v108, v109
	v_cvt_pk_f16_f32 v204, v110, v111
	v_cvt_pk_f16_f32 v205, v112, v113
	v_cvt_pk_f16_f32 v198, v98, v99
	v_cvt_pk_f16_f32 v199, v100, v101
	v_cvt_pk_f16_f32 v200, v102, v103
	v_cvt_pk_f16_f32 v201, v104, v105
	s_branch .LBB1_5
